# baseline (speedup 1.0000x reference)
.LBB1_95:
	ds_read_b32 v66, v144
	s_waitcnt lgkmcnt(0)
	v_cmp_gt_u32_e32 vcc, s10, v66
	s_cbranch_vccnz .LBB1_95
	s_branch .LBB1_88

.LBB1_100:
	ds_read_b32 v1, v0
	s_waitcnt lgkmcnt(0)
	v_cmp_lt_u32_e32 vcc, 31, v1
	s_cbranch_vccz .LBB1_100
